# BEST + dedicated conversion pass pairs horizontally adjacent units (1 KB contiguous source rows per pair)
# baseline (speedup 1.0000x reference)
; #define LAS __attribute__((address_space(3)))
; __device__ __forceinline__ void cvt8_decode(const Params& P, int L, Cvt8Unit& u) {
;     if (L < 8192) { const int up = L >= 4096; const int r_ = L & 4095; const int e = r_ >> 7, r = r_ & 127;
;         u.src = P.in[up ? 24 : 23] + (size_t)e * 2048 * 1024; u.dst = P.ws + WS_WGU + (size_t)e * 2048 * 2048; u.Kd = 2048; u.Nd = 1024; u.k0 = (r >> 3) * 128; u.n0 = (r & 7) * 128; u.nmode = up ? 2 : 1; u.scale = WGU_SCALE; return; }
;     L -= 8192;
;     { const int e = L >> 7, r = L & 127; u.src = P.in[25] + (size_t)e * 1024 * 2048; u.dst = P.ws + WS_WD + (size_t)e * 2048 * 1024; u.Kd = 1024; u.Nd = 2048; u.k0 = (r >> 4) * 128; u.n0 = (r & 15) * 128; u.nmode = 0; u.scale = WD_SCALE; }
; __device__ __forceinline__ void p0_convert_fp8(const Params& P, LAS unsigned char* lds, int tid, int blk, int G, const int Lbeg, const int Lend) {
;     LAS unsigned* tileA = (LAS unsigned*)lds;
;     LAS unsigned* tileB = tileA + 32 * 132;
;     Cvt8Unit uA, uB, nA, nB; f32x4 rA[8], rB[8], qA[8], qB[8];
;     int L = Lbeg + blk;
;     if (L >= Lend) return;
;     bool hasB = (L + G) < Lend;
;     cvt8_decode(P, L, uA); cvt8_load(uA, tid, rA);
;     if (hasB) { cvt8_decode(P, L + G, uB); cvt8_load(uB, tid, rB); }
;     for (;;) {
;         const int Ln = L + 2 * G; const bool moreA = Ln < Lend, moreB = (Ln + G) < Lend;
;         if (moreA) { cvt8_decode(P, Ln, nA); cvt8_load(nA, tid, qA); }
;         if (moreB) { cvt8_decode(P, Ln + G, nB); cvt8_load(nB, tid, qB); }
.LBB0_286:
	s_andn2_b64 vcc, exec, s[24:25]
	s_mov_b64 s[0:1], -1
	s_cbranch_vccnz .LBB0_220
	v_readlane_b32 s0, v254, 49
	s_waitcnt vmcnt(0)
	v_mov_b32_e32 v66, v0
	s_lshl_b32 s3, s2, 1
	s_mul_i32 s0, s0, s33
	s_waitcnt vmcnt(0) lgkmcnt(0)
	s_barrier
	s_lshl_b32 s64, s33, 1
	s_lshl_b32 s76, s33, 4
	s_lshl_b32 s78, s33, 8
	s_lshl_b32 s80, s33, 5
	s_add_i32 s58, s0, s64
	s_add_i32 s65, s58, 1
	s_lshl_b32 s67, s58, 3
	s_lshl_b32 s77, s58, 7
	s_lshl_b32 s79, s58, 4
	s_lshl_b32 s81, s65, 3
	s_lshl_b32 s82, s65, 7
	s_lshl_b32 s83, s65, 4
	s_add_i32 s29, s3, s0
	s_cmpk_gt_i32 s29, 0x2cff
	s_cbranch_scc1 .LBB0_219
	s_cmpk_gt_i32 s29, 0x1fff
	s_mov_b64 s[6:7], -1
	s_cbranch_scc0 .LBB0_290
	s_add_i32 s0, s29, 0xffffe000
	s_lshr_b32 s14, s0, 7
	s_lshl_b64 s[0:1], s[14:15], 23
	s_add_u32 s4, s18, s0
	s_addc_u32 s5, s19, s1
	s_lshl_b64 s[0:1], s[14:15], 21
	s_add_u32 s0, s53, s0
	s_addc_u32 s1, s54, s1
	s_lshl_b32 s6, s29, 3
	s_and_b32 s8, s6, 0x380
	s_lshl_b32 s6, s29, 7
	s_and_b32 s14, s6, 0x780
	s_mov_b64 s[6:7], 0

; __device__ __forceinline__ void cvt8_load(const Cvt8Unit& u, int tid, f32x4 (&r)[8]) {
;     const int kg = tid >> 5, nq = tid & 31;
;     const float* p = u.src + (size_t)(u.k0 + 8 * kg) * u.Nd + u.n0 + nq * 4;
; #pragma unroll
;     for (int kk = 0; kk < 8; ++kk) r[kk] = __builtin_nontemporal_load((const f32x4*)(p + (size_t)kk * u.Nd));
; }
; __device__ __forceinline__ void p0_convert_fp8(const Params& P, LAS unsigned char* lds, int tid, int blk, int G, const int Lbeg, const int Lend) {
;     ...
;     bool hasB = (L + G) < Lend;
;     cvt8_decode(P, L, uA); cvt8_load(uA, tid, rA);
;     if (hasB) { cvt8_decode(P, L + G, uB); cvt8_load(uB, tid, rB); }
;     for (;;) {
;         const int Ln = L + 2 * G; const bool moreA = Ln < Lend, moreB = (Ln + G) < Lend;
;         if (moreA) { cvt8_decode(P, Ln, nA); cvt8_load(nA, tid, qA); }
;         if (moreB) { cvt8_decode(P, Ln + G, nB); cvt8_load(nB, tid, qB); }
.LBB0_293:
	v_ashrrev_i32_e32 v134, 2, v66
	s_add_i32 s29, s29, 1
	v_and_b32_e32 v135, -8, v134
	s_cmpk_lt_i32 s29, 0x2d00
	v_add_u32_e32 v2, s8, v135
	s_cselect_b64 s[30:31], -1, 0
	s_lshl_b32 s34, s6, 2
	v_mad_i64_i32 v[2:3], s[6:7], s6, v2, 0
	v_lshlrev_b32_e32 v4, 2, v66
	v_lshl_add_u64 v[2:3], v[2:3], 2, s[4:5]
	v_and_b32_e32 v4, 0x7c, v4
	v_lshl_add_u64 v[2:3], s[14:15], 2, v[2:3]
	v_lshlrev_b32_e32 v130, 2, v4
	v_mov_b32_e32 v131, v195
	v_lshl_add_u64 v[2:3], v[2:3], 0, v[130:131]
	s_mov_b32 s35, s15
	v_lshl_add_u64 v[4:5], v[2:3], 0, s[34:35]
	global_load_dwordx4 v[62:65], v[2:3], off nt
	global_load_dwordx4 v[58:61], v[4:5], off nt
	v_lshl_add_u64 v[2:3], v[4:5], 0, s[34:35]
	v_lshl_add_u64 v[4:5], v[2:3], 0, s[34:35]
	global_load_dwordx4 v[54:57], v[2:3], off nt
	global_load_dwordx4 v[50:53], v[4:5], off nt
	v_lshl_add_u64 v[2:3], v[4:5], 0, s[34:35]
	v_lshl_add_u64 v[4:5], v[2:3], 0, s[34:35]
	global_load_dwordx4 v[46:49], v[2:3], off nt
	global_load_dwordx4 v[42:45], v[4:5], off nt
	v_lshl_add_u64 v[2:3], v[4:5], 0, s[34:35]
	v_lshl_add_u64 v[4:5], v[2:3], 0, s[34:35]
	global_load_dwordx4 v[38:41], v[2:3], off nt
	global_load_dwordx4 v[30:33], v[4:5], off nt
	s_cmpk_gt_i32 s29, 0x2cff
	s_cbranch_scc1 .LBB0_300
	s_cmpk_gt_i32 s29, 0x1fff
	s_mov_b64 s[34:35], -1
	s_cbranch_scc0 .LBB0_296
	s_add_i32 s4, s29, 0xffffe000
	s_lshr_b32 s4, s4, 7
	s_mov_b32 s5, s15
	s_lshl_b64 s[6:7], s[4:5], 23
	s_add_u32 s6, s18, s6
	s_addc_u32 s7, s19, s7
	s_lshl_b64 s[4:5], s[4:5], 21
	s_add_u32 s4, s53, s4
	s_addc_u32 s5, s54, s5
	s_lshl_b32 s28, s29, 3
	s_and_b32 s44, s28, 0x380
	s_lshl_b32 s28, s29, 7
	s_and_b32 s28, s28, 0x780
	s_mov_b64 s[34:35], 0
